# speedup vs baseline: 1.0045x; 1.0045x over previous
.LBB2_27:
	ds_read_b64_tr_b16 v[122:123], v206 offset:24576
	ds_read_b64_tr_b16 v[124:125], v206 offset:25600
	v_add_f32_e32 v66, v98, v99
	v_add_f32_e32 v66, v100, v66
	v_add_f32_e32 v66, v101, v66
	v_add_f32_e32 v66, v102, v66
	v_add_f32_e32 v82, v103, v66
	s_waitcnt lgkmcnt(9)
	v_mfma_f32_32x32x16_f16 v[66:81], v[118:121], v[154:157], v[34:49]
	v_cvt_pk_f16_f32 v158, v98, v99
	v_cvt_pk_f16_f32 v159, v100, v101
	ds_read_b64_tr_b16 v[118:119], v207 offset:24576
	ds_read_b64_tr_b16 v[120:121], v207 offset:25600
	s_waitcnt lgkmcnt(10)
	v_mfma_f32_32x32x16_f16 v[34:49], v[166:169], v[154:157], v[34:49]
	v_add_f32_e32 v82, v104, v82
	v_add_f32_e32 v82, v105, v82
	v_add_f32_e32 v82, v106, v82
	v_add_f32_e32 v82, v107, v82
	v_cvt_pk_f16_f32 v160, v102, v103
	v_cvt_pk_f16_f32 v161, v104, v105
	ds_read_b64_tr_b16 v[114:115], v206 offset:26624
	ds_read_b64_tr_b16 v[116:117], v206 offset:27648
	s_waitcnt lgkmcnt(11)
	v_mfma_f32_32x32x16_f16 v[66:81], v[170:173], v[146:149], v[66:81]
	v_add_f32_e32 v82, v108, v82
	v_add_f32_e32 v82, v109, v82
	v_add_f32_e32 v82, v110, v82
	v_add_f32_e32 v82, v111, v82
	v_cvt_pk_f16_f32 v150, v106, v107
	v_cvt_pk_f16_f32 v151, v108, v109
	ds_read_b64_tr_b16 v[102:103], v207 offset:26624
	ds_read_b64_tr_b16 v[104:105], v207 offset:27648
	s_waitcnt lgkmcnt(12)
	v_mfma_f32_32x32x16_f16 v[34:49], v[94:97], v[146:149], v[34:49]
	v_add_f32_e32 v82, v112, v82
	v_add_f32_e32 v82, v113, v82
	v_add_f32_e32 v82, v50, v82
	v_add_f32_e32 v82, v51, v82
	v_cvt_pk_f16_f32 v152, v110, v111
	v_cvt_pk_f16_f32 v153, v112, v113
	ds_read_b64_tr_b16 v[98:99], v206 offset:28672
	ds_read_b64_tr_b16 v[100:101], v206 offset:29696
	s_waitcnt lgkmcnt(13)
	v_mfma_f32_32x32x16_f16 v[66:81], v[162:165], v[138:141], v[66:81]
	v_add_f32_e32 v82, v52, v82
	v_add_f32_e32 v82, v53, v82
	v_add_f32_e32 v82, v54, v82
	v_add_f32_e32 v82, v55, v82
	v_cvt_pk_f16_f32 v142, v50, v51
	v_cvt_pk_f16_f32 v143, v52, v53
	ds_read_b64_tr_b16 v[94:95], v207 offset:28672
	ds_read_b64_tr_b16 v[96:97], v207 offset:29696
	s_waitcnt lgkmcnt(14)
	v_mfma_f32_32x32x16_f16 v[34:49], v[90:93], v[138:141], v[34:49]
	v_add_f32_e32 v50, v56, v82
	v_add_f32_e32 v50, v57, v50
	v_add_f32_e32 v50, v58, v50
	v_add_f32_e32 v50, v59, v50
	v_cvt_pk_f16_f32 v144, v54, v55
	v_cvt_pk_f16_f32 v145, v56, v57
	ds_read_b64_tr_b16 v[90:91], v206 offset:30720
	ds_read_b64_tr_b16 v[92:93], v206 offset:31744
	s_waitcnt lgkmcnt(14)
	v_mfma_f32_32x32x16_f16 v[66:81], v[126:129], v[134:137], v[66:81]
	v_add_f32_e32 v50, v60, v50
	v_add_f32_e32 v50, v61, v50
	v_add_f32_e32 v50, v62, v50
	v_add_f32_e32 v50, v63, v50
	v_cvt_pk_f16_f32 v130, v58, v59
	v_cvt_pk_f16_f32 v131, v60, v61
	ds_read_b64_tr_b16 v[82:83], v207 offset:30720
	ds_read_b64_tr_b16 v[84:85], v207 offset:31744
	v_mfma_f32_32x32x16_f16 v[34:49], v[86:89], v[134:137], v[34:49]
	v_add_f32_e32 v50, v64, v50
	v_add_f32_e32 v50, v65, v50
	v_add_f32_e32 v50, 0, v50
	v_cvt_pk_f16_f32 v132, v62, v63
	v_cvt_pk_f16_f32 v133, v64, v65
	s_cmp_lg_u32 s91, 0
	s_cbranch_scc1 .Lattn_pf_skip
	s_waitcnt lgkmcnt(0)
	s_barrier
	v_bfe_u32 v221, v0, 3, 3
	v_lshl_or_b32 v221, s33, 3, v221
	v_lshrrev_b32_e32 v222, 1, v221
	v_xor_b32_e32 v222, v222, v0
	v_lshlrev_b32_e32 v222, 4, v222
	v_and_b32_e32 v222, 0x70, v222
	v_lshl_or_b32 v221, v221, 7, v222
	s_mov_b32 m0, s36
	s_nop 0
	global_load_lds_dwordx4 v221, s[14:15]
	s_mov_b32 m0, s35
	s_nop 0
	global_load_lds_dwordx4 v[194:195], off
	s_add_u32 s44, s14, 0x2000
	s_addc_u32 s45, s15, 0
	s_add_i32 s46, s36, 0x2000
	s_mov_b32 m0, s46
	s_nop 0
	global_load_lds_dwordx4 v221, s[44:45]
	s_xor_b32 s48, s12, 0x700
	s_lshl_b32 s49, s18, 15
	s_or_b32 s48, s48, s49
	s_lshl_b32 s49, s30, 11
	s_or_b32 s48, s48, s49
	s_add_u32 s48, s48, s31
	s_mov_b32 s49, 0
	s_lshl_b64 s[48:49], s[48:49], 7
	s_add_u32 s48, s4, s48
	s_addc_u32 s49, s5, s49
	v_lshlrev_b32_e32 v223, 1, v192
	global_load_dwordx4 v[154:157], v223, s[48:49]
	global_load_dwordx4 v[146:149], v223, s[48:49] offset:32
	global_load_dwordx4 v[138:141], v223, s[48:49] offset:64
	global_load_dwordx4 v[134:137], v223, s[48:49] offset:96
	s_add_u32 s44, s14, 0x4000
	s_addc_u32 s45, s15, 0
	s_add_i32 s46, s36, 0x4000
	s_mov_b32 m0, s46
	s_nop 0
	global_load_lds_dwordx4 v221, s[44:45]
.Lattn_pf_skip:
	v_max_f32_e32 v51, v67, v67
	v_max_f32_e32 v52, v66, v66
	v_max_f32_e32 v51, v52, v51
	s_nop 3
	v_max3_f32 v52, v68, v69, v35
	v_max3_f32 v51, v51, v34, v36
	v_max3_f32 v51, v51, v37, v70
	v_max3_f32 v52, v52, v72, v73
	v_max3_f32 v51, v51, v71, v38
	v_max3_f32 v52, v52, v40, v41
	v_max3_f32 v51, v51, v39, v74
	v_max3_f32 v52, v52, v76, v77
	v_max3_f32 v51, v51, v75, v42
	v_max3_f32 v52, v52, v44, v45
	v_max3_f32 v51, v51, v43, v78
	v_max3_f32 v52, v52, v80, v81
	v_max3_f32 v51, v51, v79, v46
	v_max3_f32 v52, v52, v48, v49
	v_add_f32_e32 v86, v174, v50
	v_max3_f32 v50, v51, v47, v52
	v_mov_b32_e32 v51, v50
	s_nop 1
	v_permlane32_swap_b32_e32 v50, v51
	v_max_f32_e32 v51, v51, v51
	v_max_f32_e32 v50, v50, v50
	v_max_f32_e32 v50, v50, v51
	s_mov_b32 s2, 0x41000000
	v_cmp_lt_f32_e32 vcc, s2, v50
	s_cmp_lg_u64 vcc, 0
	s_cselect_b64 s[2:3], -1, 0
	s_cbranch_vccnz .LBB2_77

.Lattn_unit2:
	s_load_dwordx4 s[4:7], s[0:1], 0x0
	s_lshr_b32 s0, s2, 2
	s_and_b32 s3, s2, 7
	s_and_b32 s0, s0, 8
	s_or_b32 s30, s0, s3
	s_lshr_b32 s18, s2, 6
	s_mov_b32 s19, 0
	s_lshl_b32 s0, s2, 5
	v_readfirstlane_b32 s16, v0
	s_and_b32 s12, s0, 0x300
	s_xor_b32 s12, s12, s91
	s_lshl_b64 s[8:9], s[18:19], 15
	s_lshl_b32 s0, s30, 11
	s_lshr_b32 s33, s16, 6
	s_or_b32 s8, s8, s0
	s_or_b32 s0, s8, s12
	s_lshl_b32 s31, s33, 5
	s_add_u32 s0, s0, s31
	s_addc_u32 s1, s9, 0
	s_lshl_b64 s[0:1], s[0:1], 7
	s_waitcnt lgkmcnt(0)
	s_add_u32 s0, s4, s0
	s_addc_u32 s1, s5, s1
	s_lshl_b64 s[10:11], s[8:9], 7
	v_bfe_u32 v190, v0, 3, 3
	s_add_u32 s10, s4, s10
	v_lshl_or_b32 v182, s33, 3, v190
	s_addc_u32 s11, s5, s11
	v_lshrrev_b32_e32 v89, 1, v182
	s_add_u32 s14, s10, 0x1000000
	v_xor_b32_e32 v4, v89, v0
	s_addc_u32 s15, s11, 0
	v_mov_b32_e32 v183, 0
	v_lshlrev_b32_e32 v4, 4, v4
	s_add_u32 s10, s10, 0x2000000
	v_lshlrev_b64 v[86:87], 7, v[182:183]
	v_and_b32_e32 v1, 7, v0
	v_and_b32_e32 v182, 0x70, v4
	v_lshrrev_b32_e32 v4, 2, v0
	s_addc_u32 s11, s11, 0
	v_lshl_add_u64 v[2:3], s[14:15], 0, v[86:87]
	v_bitop3_b32 v4, v4, v1, 4 bitop3:0x6c
	v_lshl_add_u64 v[186:187], v[2:3], 0, v[182:183]
	v_lshl_add_u64 v[2:3], s[10:11], 0, v[86:87]
	v_lshlrev_b32_e32 v182, 4, v4
	s_lshl_b32 s36, s33, 10
	s_mov_b64 s[20:21], 0x2000
	v_and_b32_e32 v191, 31, v0
	v_lshl_add_u64 v[194:195], v[2:3], 0, v[182:183]
	s_add_i32 s35, s36, 0x6000
	v_lshl_add_u64 v[2:3], v[186:187], 0, s[20:21]
	v_bfe_u32 v88, v0, 5, 1
	s_add_i32 s37, s36, 0x2000
	v_lshlrev_b32_e32 v2, 6, v191
	v_lshl_or_b32 v192, v88, 3, v2
	v_lshlrev_b32_e32 v14, 1, v192
	v_lshrrev_b32_e32 v18, 1, v0
	s_mov_b64 s[22:23], 0x4000
	v_mov_b32_e32 v2, v183
	v_mov_b32_e32 v3, v183
	v_mov_b32_e32 v4, v183
	v_mov_b32_e32 v5, v183
	v_mov_b32_e32 v6, v183
	v_mov_b32_e32 v7, v183
	v_mov_b32_e32 v8, v183
	v_mov_b32_e32 v9, v183
	v_mov_b32_e32 v10, v183
	v_mov_b32_e32 v11, v183
	v_mov_b32_e32 v12, v183
	v_mov_b32_e32 v13, v183
	v_mov_b32_e32 v14, v183
	v_mov_b32_e32 v15, v183
	v_mov_b32_e32 v16, v183
	v_mov_b32_e32 v17, v183
	v_lshlrev_b32_e32 v38, 7, v191
	v_bitop3_b32 v18, v88, v18, 7 bitop3:0x78
	v_lshl_or_b32 v211, v18, 4, v38
	v_lshl_add_u64 v[18:19], v[186:187], 0, s[22:23]
	s_add_i32 s0, s36, 0x4000
	s_waitcnt vmcnt(4) lgkmcnt(0)
	s_barrier
	ds_read_b128 v[34:37], v211
	v_bfe_u32 v39, v0, 1, 3
	v_bitop3_b32 v40, v88, v39, 2 bitop3:0x36
	v_lshl_or_b32 v210, v40, 4, v38
	v_bitop3_b32 v40, v88, v39, 4 bitop3:0x36
	v_lshl_or_b32 v209, v40, 4, v38
	v_bitop3_b32 v39, v88, v39, 6 bitop3:0x36
	v_lshl_or_b32 v208, v39, 4, v38
	v_lshlrev_b32_e32 v201, 9, v88
	s_and_b32 s0, s16, 0x3fffffc0
	s_mov_b64 s[24:25], 0x6000
	s_lshl_b32 s38, s0, 2
	s_add_i32 s34, s36, 0x8000
	s_lshl_b32 s2, s2, 16
	s_lshl_b32 s3, s3, 18
	s_waitcnt vmcnt(4) lgkmcnt(0)
	v_mfma_f32_32x32x16_f16 v[18:33], v[34:37], v[154:157], v[2:17]
	ds_read_b128 v[34:37], v211 offset:4096
	s_and_b32 s2, s2, 0x200000
	s_lshl_b64 s[16:17], s[18:19], 22
	s_or_b32 s2, s2, s3
	s_or_b32 s16, s16, s2
	s_mov_b64 s[2:3], 0x1002000
	v_and_b32_e32 v90, 63, v0
	s_waitcnt lgkmcnt(0)
	v_mfma_f32_32x32x16_f16 v[2:17], v[34:37], v[154:157], v[2:17]
	ds_read_b128 v[34:37], v210
	s_mov_b32 s13, s19
	s_movk_i32 s42, 0x2000
	s_movk_i32 s39, 0x4000
	v_lshl_or_b32 v204, v191, 2, s38
	v_lshlrev_b32_e32 v212, 4, v88
	s_mov_b32 s40, -1
	s_waitcnt vmcnt(4) lgkmcnt(0)
	v_mfma_f32_32x32x16_f16 v[18:33], v[34:37], v[146:149], v[18:33]
	ds_read_b128 v[34:37], v210 offset:4096
	s_mov_b32 s41, 0x41000000
	s_mov_b32 s26, s19
	s_waitcnt lgkmcnt(0)
	v_mfma_f32_32x32x16_f16 v[2:17], v[34:37], v[146:149], v[2:17]
	ds_read_b128 v[34:37], v209
	s_waitcnt vmcnt(4) lgkmcnt(0)
	v_mfma_f32_32x32x16_f16 v[18:33], v[34:37], v[138:141], v[18:33]
	ds_read_b128 v[34:37], v209 offset:4096
	ds_read_b128 v[38:41], v208 offset:4096
	ds_read_b128 v[42:45], v208
	s_waitcnt lgkmcnt(2)
	v_mfma_f32_32x32x16_f16 v[2:17], v[34:37], v[138:141], v[2:17]
	v_lshlrev_b32_e32 v34, 5, v0
	v_lshlrev_b32_e32 v35, 1, v0
	v_lshlrev_b32_e32 v36, 3, v0
	v_and_b32_e32 v34, 0x180, v34
	v_and_b32_e32 v193, 24, v36
	v_and_or_b32 v34, v35, 32, v34
	v_or3_b32 v203, v34, v193, v201
	s_waitcnt vmcnt(4) lgkmcnt(0)
	v_mfma_f32_32x32x16_f16 v[18:33], v[42:45], v[134:137], v[18:33]
	v_and_b32_e32 v200, 64, v36
	v_bitop3_b32 v202, v36, 64, v36 bitop3:0xc
	v_or_b32_e32 v206, v203, v200
	v_or_b32_e32 v207, v203, v202
	v_mfma_f32_32x32x16_f16 v[2:17], v[38:41], v[134:137], v[2:17]
	s_nop 15
	s_nop 7
	s_nop 0
	v_max3_f32 v34, v18, v19, v2
	v_max3_f32 v35, v20, v21, v3
	s_nop 0
	v_max3_f32 v34, v34, v4, v5
	v_max3_f32 v35, v35, v24, v25
	s_nop 0
	v_max3_f32 v34, v34, v22, v23
	v_max3_f32 v35, v35, v8, v9
	s_nop 0
	v_max3_f32 v34, v34, v6, v7
	v_max3_f32 v35, v35, v28, v29
	s_nop 0
	v_max3_f32 v34, v34, v26, v27
	v_max3_f32 v35, v35, v12, v13
	s_nop 0
	v_max3_f32 v34, v34, v10, v11
	v_max3_f32 v35, v35, v32, v33
	s_nop 0
	v_max3_f32 v34, v34, v30, v31
	v_max3_f32 v35, v35, v16, v17
	s_nop 0
	v_max3_f32 v34, v34, v14, v15
	s_nop 0
	v_max_f32_e32 v34, v34, v35
	s_nop 0
	v_mov_b32_e32 v35, v34
	s_nop 1
	v_permlane32_swap_b32_e32 v34, v35
	v_max_f32_e32 v34, v34, v35
	s_nop 0
	v_add_f32_e32 v205, v183, v34
	v_sub_f32_e32 v18, v18, v34
	v_sub_f32_e32 v2, v2, v34
	v_sub_f32_e32 v19, v19, v34
	v_sub_f32_e32 v3, v3, v34
	v_sub_f32_e32 v20, v20, v34
	v_sub_f32_e32 v4, v4, v34
	v_sub_f32_e32 v21, v21, v34
	v_sub_f32_e32 v5, v5, v34
	v_sub_f32_e32 v22, v22, v34
	v_sub_f32_e32 v6, v6, v34
	v_sub_f32_e32 v23, v23, v34
	v_sub_f32_e32 v7, v7, v34
	v_sub_f32_e32 v24, v24, v34
	v_sub_f32_e32 v8, v8, v34
	v_sub_f32_e32 v25, v25, v34
	v_sub_f32_e32 v9, v9, v34
	v_sub_f32_e32 v26, v26, v34
	v_sub_f32_e32 v10, v10, v34
	v_sub_f32_e32 v27, v27, v34
	v_sub_f32_e32 v11, v11, v34
	v_sub_f32_e32 v28, v28, v34
	v_sub_f32_e32 v12, v12, v34
	v_sub_f32_e32 v29, v29, v34
	v_sub_f32_e32 v13, v13, v34
	v_sub_f32_e32 v30, v30, v34
	v_sub_f32_e32 v14, v14, v34
	v_sub_f32_e32 v31, v31, v34
	v_sub_f32_e32 v15, v15, v34
	v_sub_f32_e32 v32, v32, v34
	v_sub_f32_e32 v16, v16, v34
	v_sub_f32_e32 v33, v33, v34
	v_sub_f32_e32 v17, v17, v34
	s_nop 0
	v_xor_b32_e32 v34, 0x80000000, v205
	v_mov_b32_e32 v35, v34
	v_mov_b32_e32 v36, v34
	v_mov_b32_e32 v37, v34
	v_mov_b32_e32 v38, v34
	v_mov_b32_e32 v39, v34
	v_mov_b32_e32 v40, v34
	v_mov_b32_e32 v41, v34
	v_mov_b32_e32 v42, v34
	v_mov_b32_e32 v43, v34
	v_mov_b32_e32 v44, v34
	v_mov_b32_e32 v45, v34
	v_mov_b32_e32 v46, v34
	v_mov_b32_e32 v47, v34
	v_mov_b32_e32 v48, v34
	v_mov_b32_e32 v49, v34
	s_waitcnt vmcnt(0) lgkmcnt(0)
	s_barrier
	v_exp_f32_e32 v50, v2
	v_exp_f32_e32 v51, v3
	v_lshl_add_u64 v[2:3], v[186:187], 0, s[24:25]
	s_mov_b32 s0, m0
	s_mov_b32 m0, s36
	s_nop 0
	global_load_lds_dwordx4 v[2:3], off
	s_mov_b32 m0, s0
	v_lshl_add_u64 v[2:3], v[194:195], 0, s[20:21]
	s_mov_b32 s0, m0
	s_mov_b32 m0, s34
	s_nop 0
	global_load_lds_dwordx4 v[2:3], off
	s_mov_b32 m0, s0
	ds_read_b128 v[82:85], v211 offset:8192
	ds_read_b128 v[170:173], v211 offset:12288
	ds_read_b128 v[166:169], v210 offset:8192
	ds_read_b128 v[162:165], v210 offset:12288
	ds_read_b128 v[126:129], v209 offset:8192
	ds_read_b128 v[122:125], v209 offset:12288
	ds_read_b128 v[118:121], v208 offset:8192
	ds_read_b128 v[114:117], v208 offset:12288
	v_exp_f32_e32 v52, v4
	v_lshl_add_u64 v[2:3], s[16:17], 0, v[86:87]
	v_bitop3_b32 v4, v89, 7, v0 bitop3:0x48
	v_exp_f32_e32 v66, v18
	v_exp_f32_e32 v67, v19
	v_exp_f32_e32 v68, v20
	v_exp_f32_e32 v69, v21
	v_exp_f32_e32 v70, v22
	v_exp_f32_e32 v71, v23
	v_exp_f32_e32 v72, v24
	v_exp_f32_e32 v73, v25
	v_exp_f32_e32 v74, v26
	v_exp_f32_e32 v75, v27
	v_exp_f32_e32 v76, v28
	v_exp_f32_e32 v77, v29
	v_exp_f32_e32 v78, v30
	v_exp_f32_e32 v79, v31
	v_exp_f32_e32 v80, v32
	v_exp_f32_e32 v81, v33
	v_exp_f32_e32 v53, v5
	v_exp_f32_e32 v54, v6
	v_exp_f32_e32 v55, v7
	v_exp_f32_e32 v56, v8
	v_exp_f32_e32 v57, v9
	v_exp_f32_e32 v58, v10
	v_exp_f32_e32 v59, v11
	v_exp_f32_e32 v60, v12
	v_exp_f32_e32 v61, v13
	v_exp_f32_e32 v62, v14
	v_exp_f32_e32 v63, v15
	v_exp_f32_e32 v64, v16
	v_exp_f32_e32 v65, v17
	v_lshl_or_b32 v4, v4, 4, v2
	v_mov_b32_e32 v5, v3
	s_waitcnt vmcnt(2) lgkmcnt(0)
	s_barrier
	v_lshl_add_u64 v[4:5], s[4:5], 0, v[4:5]
	v_or_b32_e32 v2, v2, v182
	v_lshl_add_u64 v[188:189], v[4:5], 0, s[2:3]
	v_lshl_add_u64 v[2:3], s[4:5], 0, v[2:3]
	s_mov_b64 s[2:3], 0x2002000
	v_cmp_gt_u32_e64 s[0:1], 32, v90
	v_lshl_add_u64 v[196:197], v[2:3], 0, s[2:3]
	s_mov_b64 s[2:3], 0x8000
	v_mov_b32_e32 v2, v183
	v_mov_b32_e32 v3, v183
	v_mov_b32_e32 v4, v183
	v_mov_b32_e32 v5, v183
	v_mov_b32_e32 v6, v183
	v_mov_b32_e32 v7, v183
	v_mov_b32_e32 v8, v183
	v_mov_b32_e32 v9, v183
	v_mov_b32_e32 v10, v183
	v_mov_b32_e32 v11, v183
	v_mov_b32_e32 v12, v183
	v_mov_b32_e32 v13, v183
	v_mov_b32_e32 v14, v183
	v_mov_b32_e32 v15, v183
	v_mov_b32_e32 v16, v183
	v_mov_b32_e32 v17, v183
	v_mov_b32_e32 v18, v183
	v_mov_b32_e32 v19, v183
	v_mov_b32_e32 v20, v183
	v_mov_b32_e32 v21, v183
	v_mov_b32_e32 v22, v183
	v_mov_b32_e32 v23, v183
	v_mov_b32_e32 v24, v183
	v_mov_b32_e32 v25, v183
	v_mov_b32_e32 v26, v183
	v_mov_b32_e32 v27, v183
	v_mov_b32_e32 v28, v183
	v_mov_b32_e32 v29, v183
	v_mov_b32_e32 v30, v183
	v_mov_b32_e32 v31, v183
	v_mov_b32_e32 v32, v183
	v_mov_b32_e32 v33, v183
	s_branch .LBB2_1

	.amdhsa_kernel _ZN4attn8attn_fwdEPKDF16_PDF16_
		.amdhsa_group_segment_fixed_size 83968
		.amdhsa_private_segment_fixed_size 0
		.amdhsa_kernarg_size 16
		.amdhsa_user_sgpr_count 2
		.amdhsa_user_sgpr_dispatch_ptr 0
		.amdhsa_user_sgpr_queue_ptr 0
		.amdhsa_user_sgpr_kernarg_segment_ptr 1
		.amdhsa_user_sgpr_dispatch_id 0
		.amdhsa_user_sgpr_kernarg_preload_length 0
		.amdhsa_user_sgpr_kernarg_preload_offset 0
		.amdhsa_user_sgpr_private_segment_size 0
		.amdhsa_uses_dynamic_stack 0
		.amdhsa_enable_private_segment 0
		.amdhsa_system_sgpr_workgroup_id_x 1
		.amdhsa_system_sgpr_workgroup_id_y 0
		.amdhsa_system_sgpr_workgroup_id_z 0
		.amdhsa_system_sgpr_workgroup_info 0
		.amdhsa_system_vgpr_workitem_id 0
		.amdhsa_next_free_vgpr 224
		.amdhsa_next_free_sgpr 96
		.amdhsa_accum_offset 224
		.amdhsa_reserve_vcc 1
		.amdhsa_float_round_mode_32 0
		.amdhsa_float_round_mode_16_64 0
		.amdhsa_float_denorm_mode_32 3
		.amdhsa_float_denorm_mode_16_64 3
		.amdhsa_dx10_clamp 1
		.amdhsa_ieee_mode 1
		.amdhsa_fp16_overflow 0
		.amdhsa_tg_split 0
		.amdhsa_exception_fp_ieee_invalid_op 0
		.amdhsa_exception_fp_denorm_src 0
		.amdhsa_exception_fp_ieee_div_zero 0
		.amdhsa_exception_fp_ieee_overflow 0
		.amdhsa_exception_fp_ieee_underflow 0
		.amdhsa_exception_fp_ieee_inexact 0
		.amdhsa_exception_int_div_zero 0
	.end_amdhsa_kernel
